# variant: z0/z1 prefetch (pieces 3-7) + sc1 loads + invalidates removed, without the Y prefetch
# baseline (speedup 1.0000x reference)
;     __device__ __forceinline__ void operator()(const f32x4 (&acc)[2][2][4][2], const Unit& u, int wr, int wc, int fr, int fq) const {
;     ...
;             for (int m = 2 * mp; m < 2 * mp + 2; ++m) { const size_t off = offa + (size_t)m * 16 * 1024;
;                 f16x8 za[2], zb[2];
;                 if (br == 2) {
; #pragma unroll
;                     for (int bj = 0; bj < 2; ++bj) { za[bj] = *(const g_f16x8*)(Y + off + bj * HALF); zb[bj] = *(const g_f16x8*)(Y + YSTR + off + bj * HALF); } }
.LBB0_1239:
	v_cvt_pk_f16_f32 v180, v166, v167
	v_cvt_pk_f16_f32 v181, v172, v173
	v_cvt_pk_f16_f32 v182, v170, v171
	v_cvt_pk_f16_f32 v183, v168, v169
	s_and_b64 vcc, exec, s[36:37]
	global_store_dwordx4 v[178:179], v[180:183], off offset:256
	s_cbranch_vccnz .LBB0_1241
	v_mov_b64_e32 v[42:43], 0x8000
	v_lshl_add_u64 v[42:43], v[228:229], 1, v[42:43]
	v_lshl_add_u64 v[44:45], s[40:41], 0, v[42:43]
	s_waitcnt vmcnt(2)
	v_lshl_add_u64 v[46:47], s[44:45], 0, v[42:43]
	global_load_dwordx4 v[58:61], v[44:45], off sc1
	s_nop 0
	global_load_dwordx4 v[42:45], v[44:45], off offset:256 sc1
	s_nop 0
	global_load_dwordx4 v[66:69], v[46:47], off sc1
	s_nop 0
	global_load_dwordx4 v[46:49], v[46:47], off offset:256 sc1

;     __device__ __forceinline__ void operator()(const f32x4 (&acc)[2][2][4][2], const Unit& u, int wr, int wc, int fr, int fq) const {
;     ...
;             for (int mp = 0; mp < 2; ++mp) {
;             f16x8 yv[4][2];
; #pragma unroll
;             for (int m = 2 * mp; m < 2 * mp + 2; ++m)
; #pragma unroll
;                 for (int bj = 0; bj < 2; ++bj) yv[m][bj] = *(const g_f16x8*)(Yb + offa + (size_t)m * 16 * 1024 + bj * HALF);
; #pragma unroll
;             for (int m = 2 * mp; m < 2 * mp + 2; ++m) { const size_t off = offa + (size_t)m * 16 * 1024;
;                 f16x8 za[2], zb[2];
;                 if (br == 2) {
; #pragma unroll
;                     for (int bj = 0; bj < 2; ++bj) { za[bj] = *(const g_f16x8*)(Y + off + bj * HALF); zb[bj] = *(const g_f16x8*)(Y + YSTR + off + bj * HALF); } }
.LBB0_1247:
	s_mov_b64 s[28:29], 0x8000
	v_lshl_add_u64 v[158:159], v[178:179], 0, s[28:29]
	v_cvt_pk_f16_f32 v154, v146, v147
	v_cvt_pk_f16_f32 v155, v152, v153
	v_cvt_pk_f16_f32 v156, v150, v151
	v_cvt_pk_f16_f32 v157, v148, v149
	v_add_co_u32_e32 v146, vcc, 0x10000, v224
	global_store_dwordx4 v[158:159], v[154:157], off offset:256
	s_nop 0
	v_addc_co_u32_e32 v147, vcc, 0, v225, vcc
	global_load_dwordx4 v[158:161], v[146:147], off sc1
	global_load_dwordx4 v[154:157], v[146:147], off offset:256 sc1
	v_add_co_u32_e32 v146, vcc, 0x18000, v224
	s_nop 1
	v_addc_co_u32_e32 v147, vcc, 0, v225, vcc
	global_load_dwordx4 v[150:153], v[146:147], off sc1
	s_nop 0
	global_load_dwordx4 v[146:149], v[146:147], off offset:256 sc1
	s_and_b64 vcc, exec, s[36:37]
	s_cbranch_vccnz .LBB0_1249
	v_mov_b64_e32 v[42:43], 0x10000
	v_lshl_add_u64 v[42:43], v[228:229], 1, v[42:43]
	v_lshl_add_u64 v[44:45], s[40:41], 0, v[42:43]
	s_waitcnt vmcnt(6)
	v_lshl_add_u64 v[46:47], s[44:45], 0, v[42:43]
	global_load_dwordx4 v[58:61], v[44:45], off sc1
	s_nop 0
	global_load_dwordx4 v[42:45], v[44:45], off offset:256 sc1
	s_nop 0
	global_load_dwordx4 v[66:69], v[46:47], off sc1
	s_nop 0
	global_load_dwordx4 v[46:49], v[46:47], off offset:256 sc1
	s_mov_b64 s[28:29], 0x18000
	v_lshl_add_u64 v[180:181], v[228:229], 1, s[28:29]
	v_lshl_add_u64 v[246:247], s[44:45], 0, v[180:181]
	v_lshl_add_u64 v[180:181], s[40:41], 0, v[180:181]
	global_load_dwordx4 v[174:177], v[180:181], off sc1
	global_load_dwordx4 v[180:183], v[180:181], off offset:256 sc1
	global_load_dwordx4 v[238:241], v[246:247], off sc1
	global_load_dwordx4 v[246:249], v[246:247], off offset:256 sc1

;     __device__ __forceinline__ void operator()(const f32x4 (&acc)[2][2][4][2], const Unit& u, int wr, int wc, int fr, int fq) const {
;     ...
;             for (int m = 2 * mp; m < 2 * mp + 2; ++m) { const size_t off = offa + (size_t)m * 16 * 1024;
;                 f16x8 za[2], zb[2];
;                 if (br == 2) {
; #pragma unroll
;                     for (int bj = 0; bj < 2; ++bj) { za[bj] = *(const g_f16x8*)(Y + off + bj * HALF); zb[bj] = *(const g_f16x8*)(Y + YSTR + off + bj * HALF); } }
.LBB0_1255:
	s_mov_b64 s[28:29], 0x10000
	v_lshl_add_u64 v[142:143], v[178:179], 0, s[28:29]
	v_cvt_pk_f16_f32 v138, v130, v131
	v_cvt_pk_f16_f32 v139, v136, v137
	v_cvt_pk_f16_f32 v140, v134, v135
	v_cvt_pk_f16_f32 v141, v132, v133
	s_and_b64 vcc, exec, s[36:37]
	global_store_dwordx4 v[142:143], v[138:141], off offset:256
	s_cbranch_vccnz .LBB0_1257
	v_mov_b64_e32 v[42:43], 0x18000
	v_lshl_add_u64 v[42:43], v[228:229], 1, v[42:43]
	v_lshl_add_u64 v[44:45], s[40:41], 0, v[42:43]
	s_waitcnt vmcnt(6)
	v_lshl_add_u64 v[46:47], s[44:45], 0, v[42:43]
	s_nop 0
	s_nop 0
	s_nop 0
	s_mov_b64 s[28:29], 0x40000
	v_lshl_add_u64 v[158:159], v[228:229], 1, s[28:29]
	v_lshl_add_u64 v[166:167], s[44:45], 0, v[158:159]
	v_lshl_add_u64 v[158:159], s[40:41], 0, v[158:159]
	global_load_dwordx4 v[154:157], v[158:159], off sc1
	global_load_dwordx4 v[158:161], v[158:159], off offset:256 sc1
	global_load_dwordx4 v[162:165], v[166:167], off sc1
	global_load_dwordx4 v[166:169], v[166:167], off offset:256 sc1

;     __device__ __forceinline__ void operator()(const f32x4 (&acc)[2][2][4][2], const Unit& u, int wr, int wc, int fr, int fq) const {
;     ...
;             const int rowa = row0 + ai * HALF; const size_t offa = (size_t)rowa * 1024 + (size_t)(rowa >> 12) * GAPY + col0;
; #pragma unroll
;             for (int mp = 0; mp < 2; ++mp) {
;             f16x8 yv[4][2];
; #pragma unroll
;             for (int m = 2 * mp; m < 2 * mp + 2; ++m)
; #pragma unroll
;                 for (int bj = 0; bj < 2; ++bj) yv[m][bj] = *(const g_f16x8*)(Yb + offa + (size_t)m * 16 * 1024 + bj * HALF);
; #pragma unroll
;             for (int m = 2 * mp; m < 2 * mp + 2; ++m) { const size_t off = offa + (size_t)m * 16 * 1024;
;                 f16x8 za[2], zb[2];
;                 if (br == 2) {
; #pragma unroll
;                     for (int bj = 0; bj < 2; ++bj) { za[bj] = *(const g_f16x8*)(Y + off + bj * HALF); zb[bj] = *(const g_f16x8*)(Y + YSTR + off + bj * HALF); } }
.LBB0_1263:
	v_cvt_pk_f16_f32 v122, v114, v115
	v_add_u32_e32 v114, 0x80, v218
	v_ashrrev_i32_e32 v115, 31, v114
	v_cvt_pk_f16_f32 v125, v116, v117
	v_lshlrev_b64 v[116:117], 10, v[114:115]
	v_cvt_pk_f16_f32 v124, v118, v119
	v_ashrrev_i32_e32 v118, 12, v114
	v_lshl_add_u64 v[114:115], v[116:117], 0, v[216:217]
	s_mov_b32 s26, 0xc00000
	v_mad_i64_i32 v[130:131], s[50:51], v118, s26, v[114:115]
	s_mov_b64 s[28:29], 0x18000
	v_lshl_add_u64 v[132:133], v[130:131], 1, s[48:49]
	v_lshl_add_u64 v[126:127], v[178:179], 0, s[28:29]
	v_cvt_pk_f16_f32 v123, v120, v121
	v_add_co_u32_e32 v114, vcc, 0x8000, v132
	global_store_dwordx4 v[126:127], v[122:125], off offset:256
	s_nop 0
	v_addc_co_u32_e32 v115, vcc, 0, v133, vcc
	global_load_dwordx4 v[126:129], v[132:133], off sc1
	global_load_dwordx4 v[122:125], v[132:133], off offset:256 sc1
	global_load_dwordx4 v[118:121], v[114:115], off sc1
	s_nop 0
	global_load_dwordx4 v[114:117], v[114:115], off offset:256 sc1
	s_and_b64 vcc, exec, s[36:37]
	s_cbranch_vccnz .LBB0_1265
	v_lshlrev_b64 v[42:43], 1, v[130:131]
	v_lshl_add_u64 v[44:45], s[40:41], 0, v[42:43]
	s_waitcnt vmcnt(14)
	v_lshl_add_u64 v[46:47], s[44:45], 0, v[42:43]
	s_nop 0
	s_nop 0
	s_nop 0
	s_mov_b64 s[28:29], 0x48000
	v_lshl_add_u64 v[150:151], v[228:229], 1, s[28:29]
	v_lshl_add_u64 v[220:221], s[44:45], 0, v[150:151]
	v_lshl_add_u64 v[150:151], s[40:41], 0, v[150:151]
	global_load_dwordx4 v[146:149], v[150:151], off sc1
	global_load_dwordx4 v[150:153], v[150:151], off offset:256 sc1
	global_load_dwordx4 v[216:219], v[220:221], off sc1
	global_load_dwordx4 v[220:223], v[220:221], off offset:256 sc1
	s_mov_b64 s[28:29], 0x50000
	v_lshl_add_u64 v[174:175], v[228:229], 1, s[28:29]
	v_lshl_add_u64 v[224:225], s[44:45], 0, v[174:175]
	v_lshl_add_u64 v[174:175], s[40:41], 0, v[174:175]
	global_load_dwordx4 v[170:173], v[174:175], off sc1
	global_load_dwordx4 v[174:177], v[174:175], off offset:256 sc1
	global_load_dwordx4 v[178:181], v[224:225], off sc1
	global_load_dwordx4 v[224:227], v[224:225], off offset:256 sc1

;     __device__ __forceinline__ void operator()(const f32x4 (&acc)[2][2][4][2], const Unit& u, int wr, int wc, int fr, int fq) const {
;     ...
;             for (int m = 2 * mp; m < 2 * mp + 2; ++m) { const size_t off = offa + (size_t)m * 16 * 1024;
;                 f16x8 za[2], zb[2];
;                 if (br == 2) {
; #pragma unroll
;                     for (int bj = 0; bj < 2; ++bj) { za[bj] = *(const g_f16x8*)(Y + off + bj * HALF); zb[bj] = *(const g_f16x8*)(Y + YSTR + off + bj * HALF); } }
.LBB0_1271:
	v_cvt_pk_f16_f32 v108, v98, v99
	v_cvt_pk_f16_f32 v109, v104, v105
	v_cvt_pk_f16_f32 v110, v102, v103
	v_cvt_pk_f16_f32 v111, v100, v101
	s_and_b64 vcc, exec, s[36:37]
	global_store_dwordx4 v[106:107], v[108:111], off offset:256
	s_cbranch_vccnz .LBB0_1273
	v_mov_b64_e32 v[42:43], 0x8000
	v_lshl_add_u64 v[42:43], v[130:131], 1, v[42:43]
	v_lshl_add_u64 v[44:45], s[40:41], 0, v[42:43]
	s_waitcnt vmcnt(16)
	v_lshl_add_u64 v[46:47], s[44:45], 0, v[42:43]
	s_nop 0
	s_nop 0
	s_nop 0
	s_mov_b64 s[28:29], 0x58000
	v_lshl_add_u64 v[158:159], v[228:229], 1, s[28:29]
	v_lshl_add_u64 v[166:167], s[44:45], 0, v[158:159]
	v_lshl_add_u64 v[158:159], s[40:41], 0, v[158:159]
	global_load_dwordx4 v[154:157], v[158:159], off sc1
	global_load_dwordx4 v[158:161], v[158:159], off offset:256 sc1
	global_load_dwordx4 v[162:165], v[166:167], off sc1
	global_load_dwordx4 v[166:169], v[166:167], off offset:256 sc1

;     __device__ __forceinline__ void operator()(const f32x4 (&acc)[2][2][4][2], const Unit& u, int wr, int wc, int fr, int fq) const {
;     ...
;             for (int mp = 0; mp < 2; ++mp) {
;             f16x8 yv[4][2];
; #pragma unroll
;             for (int m = 2 * mp; m < 2 * mp + 2; ++m)
; #pragma unroll
;                 for (int bj = 0; bj < 2; ++bj) yv[m][bj] = *(const g_f16x8*)(Yb + offa + (size_t)m * 16 * 1024 + bj * HALF);
; #pragma unroll
;             for (int m = 2 * mp; m < 2 * mp + 2; ++m) { const size_t off = offa + (size_t)m * 16 * 1024;
;                 f16x8 za[2], zb[2];
;                 if (br == 2) {
; #pragma unroll
;                     for (int bj = 0; bj < 2; ++bj) { za[bj] = *(const g_f16x8*)(Y + off + bj * HALF); zb[bj] = *(const g_f16x8*)(Y + YSTR + off + bj * HALF); } }
.LBB0_1279:
	s_mov_b64 s[28:29], 0x8000
	v_lshl_add_u64 v[94:95], v[106:107], 0, s[28:29]
	v_cvt_pk_f16_f32 v90, v82, v83
	v_cvt_pk_f16_f32 v91, v88, v89
	v_cvt_pk_f16_f32 v92, v86, v87
	v_cvt_pk_f16_f32 v93, v84, v85
	v_add_co_u32_e32 v82, vcc, 0x10000, v132
	global_store_dwordx4 v[94:95], v[90:93], off offset:256
	s_nop 0
	v_addc_co_u32_e32 v83, vcc, 0, v133, vcc
	global_load_dwordx4 v[94:97], v[82:83], off sc1
	global_load_dwordx4 v[90:93], v[82:83], off offset:256 sc1
	v_add_co_u32_e32 v82, vcc, 0x18000, v132
	s_nop 1
	v_addc_co_u32_e32 v83, vcc, 0, v133, vcc
	global_load_dwordx4 v[86:89], v[82:83], off sc1
	s_nop 0
	global_load_dwordx4 v[82:85], v[82:83], off offset:256 sc1
	s_and_b64 vcc, exec, s[36:37]
	s_cbranch_vccnz .LBB0_1281
	v_mov_b64_e32 v[42:43], 0x10000
	v_lshl_add_u64 v[42:43], v[130:131], 1, v[42:43]
	v_lshl_add_u64 v[44:45], s[40:41], 0, v[42:43]
	s_waitcnt vmcnt(36)
	v_lshl_add_u64 v[46:47], s[44:45], 0, v[42:43]
	s_nop 0
	s_nop 0
	s_nop 0
